# hand-written interleaved piece search + counting atomics in k_bucket, on top of rank sort rewrite
# baseline (speedup 1.0000x reference)
.Lw1b33:
	s_movk_i32 s57, 0x2000
	s_and_b64 vcc, exec, s[34:35]
	s_cbranch_vccz .LBB1_231
	s_waitcnt lgkmcnt(0)
	s_mov_b32 s34, 0x11800
	s_movk_i32 s35, 0x62
	v_mov_b32_e32 v32, v0
	v_add_u32_e32 v33, 1024, v0
	v_add_u32_e32 v34, 2048, v0
	v_add_u32_e32 v35, 3072, v0

.Lw1b34:
	v_add_u32_e32 v36, 4096, v0
	v_add_u32_e32 v37, 5120, v0
	v_add_u32_e32 v38, 6144, v0
	v_add_u32_e32 v39, 7168, v0
	v_cmp_le_i32_e64 s[36:37], v5, v32
	v_cmp_le_i32_e64 s[38:39], v5, v33
	v_cmp_le_i32_e64 s[58:59], v5, v34
	v_cmp_le_i32_e64 s[60:61], v5, v35

.Lw1b35:
	v_cndmask_b32_e64 v40, 0, 64, s[36:37]
	v_cndmask_b32_e64 v41, 0, 64, s[38:39]
	v_cndmask_b32_e64 v42, 0, 64, s[58:59]
	v_cndmask_b32_e64 v43, 0, 64, s[60:61]
	v_cmp_le_i32_e64 s[36:37], v5, v36
	v_cmp_le_i32_e64 s[38:39], v5, v37
	v_cmp_le_i32_e64 s[58:59], v5, v38

.Lw1b36:
	v_cmp_le_i32_e64 s[60:61], v5, v39
	v_cndmask_b32_e64 v44, 0, 64, s[36:37]
	v_cndmask_b32_e64 v45, 0, 64, s[38:39]
	v_cndmask_b32_e64 v46, 0, 64, s[58:59]
	v_cndmask_b32_e64 v47, 0, 64, s[60:61]
	v_add_u32_e32 v3, 32, v40
	v_lshl_add_u32 v11, v3, 2, s34
	ds_read_b32 v11, v11

.Lw1b37:
	v_add_u32_e32 v4, 32, v41
	v_lshl_add_u32 v12, v4, 2, s34
	ds_read_b32 v12, v12
	v_add_u32_e32 v6, 32, v42
	v_lshl_add_u32 v13, v6, 2, s34
	ds_read_b32 v13, v13
	v_add_u32_e32 v7, 32, v43
	v_lshl_add_u32 v14, v7, 2, s34
	ds_read_b32 v14, v14

.Lw1b38:
	v_add_u32_e32 v8, 32, v44
	v_lshl_add_u32 v15, v8, 2, s34
	ds_read_b32 v15, v15
	v_add_u32_e32 v9, 32, v45
	v_lshl_add_u32 v16, v9, 2, s34
	ds_read_b32 v16, v16
	v_add_u32_e32 v10, 32, v46
	v_lshl_add_u32 v17, v10, 2, s34
	ds_read_b32 v17, v17

.Lw1b39:
	v_add_u32_e32 v19, 32, v47
	v_lshl_add_u32 v18, v19, 2, s34
	ds_read_b32 v18, v18
	s_waitcnt lgkmcnt(7)
	v_cmp_le_i32_e64 s[36:37], v11, v32
	s_waitcnt lgkmcnt(6)
	v_cmp_le_i32_e64 s[38:39], v12, v33
	s_waitcnt lgkmcnt(5)
	v_cmp_le_i32_e64 s[58:59], v13, v34
	s_waitcnt lgkmcnt(4)

.Lw1b40:
	v_cmp_le_i32_e64 s[60:61], v14, v35
	v_cndmask_b32_e64 v40, v40, v3, s[36:37]
	v_cndmask_b32_e64 v41, v41, v4, s[38:39]
	v_cndmask_b32_e64 v42, v42, v6, s[58:59]
	v_cndmask_b32_e64 v43, v43, v7, s[60:61]
	s_waitcnt lgkmcnt(3)
	v_cmp_le_i32_e64 s[36:37], v15, v36
	s_waitcnt lgkmcnt(2)
	v_cmp_le_i32_e64 s[38:39], v16, v37

.Lw1b41:
	s_waitcnt lgkmcnt(1)
	v_cmp_le_i32_e64 s[58:59], v17, v38
	s_waitcnt lgkmcnt(0)
	v_cmp_le_i32_e64 s[60:61], v18, v39
	v_cndmask_b32_e64 v44, v44, v8, s[36:37]
	v_cndmask_b32_e64 v45, v45, v9, s[38:39]
	v_cndmask_b32_e64 v46, v46, v10, s[58:59]
	v_cndmask_b32_e64 v47, v47, v19, s[60:61]

.Lw1b42:
	v_add_u32_e32 v3, 16, v40
	v_min_u32_e32 v11, s35, v3
	v_lshl_add_u32 v11, v11, 2, s34
	ds_read_b32 v11, v11
	v_add_u32_e32 v4, 16, v41
	v_min_u32_e32 v12, s35, v4
	v_lshl_add_u32 v12, v12, 2, s34
	ds_read_b32 v12, v12
	v_add_u32_e32 v6, 16, v42
	v_min_u32_e32 v13, s35, v6
	v_lshl_add_u32 v13, v13, 2, s34

.Lw1b43:
	ds_read_b32 v13, v13
	v_add_u32_e32 v7, 16, v43
	v_min_u32_e32 v14, s35, v7
	v_lshl_add_u32 v14, v14, 2, s34
	ds_read_b32 v14, v14
	v_add_u32_e32 v8, 16, v44
	v_min_u32_e32 v15, s35, v8
	v_lshl_add_u32 v15, v15, 2, s34
	ds_read_b32 v15, v15

.Lw1b44:
	v_add_u32_e32 v9, 16, v45
	v_min_u32_e32 v16, s35, v9
	v_lshl_add_u32 v16, v16, 2, s34
	ds_read_b32 v16, v16
	v_add_u32_e32 v10, 16, v46
	v_min_u32_e32 v17, s35, v10
	v_lshl_add_u32 v17, v17, 2, s34
	ds_read_b32 v17, v17
	v_add_u32_e32 v19, 16, v47
	v_min_u32_e32 v18, s35, v19
	v_lshl_add_u32 v18, v18, 2, s34

.Lw1b45:
	ds_read_b32 v18, v18
	s_waitcnt lgkmcnt(7)
	v_cmp_le_i32_e64 s[36:37], v11, v32
	s_waitcnt lgkmcnt(6)
	v_cmp_le_i32_e64 s[38:39], v12, v33
	s_waitcnt lgkmcnt(5)
	v_cmp_le_i32_e64 s[58:59], v13, v34
	s_waitcnt lgkmcnt(4)
	v_cmp_le_i32_e64 s[60:61], v14, v35

.Lw1b46:
	v_cndmask_b32_e64 v40, v40, v3, s[36:37]
	v_cndmask_b32_e64 v41, v41, v4, s[38:39]
	v_cndmask_b32_e64 v42, v42, v6, s[58:59]
	v_cndmask_b32_e64 v43, v43, v7, s[60:61]
	s_waitcnt lgkmcnt(3)
	v_cmp_le_i32_e64 s[36:37], v15, v36
	s_waitcnt lgkmcnt(2)
	v_cmp_le_i32_e64 s[38:39], v16, v37
	s_waitcnt lgkmcnt(1)

.Lw1b47:
	v_cmp_le_i32_e64 s[58:59], v17, v38
	s_waitcnt lgkmcnt(0)
	v_cmp_le_i32_e64 s[60:61], v18, v39
	v_cndmask_b32_e64 v44, v44, v8, s[36:37]
	v_cndmask_b32_e64 v45, v45, v9, s[38:39]
	v_cndmask_b32_e64 v46, v46, v10, s[58:59]
	v_cndmask_b32_e64 v47, v47, v19, s[60:61]
	v_add_u32_e32 v3, 8, v40
	v_min_u32_e32 v11, s35, v3

.Lw1b48:
	v_lshl_add_u32 v11, v11, 2, s34
	ds_read_b32 v11, v11
	v_add_u32_e32 v4, 8, v41
	v_min_u32_e32 v12, s35, v4
	v_lshl_add_u32 v12, v12, 2, s34
	ds_read_b32 v12, v12
	v_add_u32_e32 v6, 8, v42
	v_min_u32_e32 v13, s35, v6
	v_lshl_add_u32 v13, v13, 2, s34
	ds_read_b32 v13, v13

.Lw1b49:
	v_add_u32_e32 v7, 8, v43
	v_min_u32_e32 v14, s35, v7
	v_lshl_add_u32 v14, v14, 2, s34
	ds_read_b32 v14, v14
	v_add_u32_e32 v8, 8, v44
	v_min_u32_e32 v15, s35, v8
	v_lshl_add_u32 v15, v15, 2, s34
	ds_read_b32 v15, v15
	v_add_u32_e32 v9, 8, v45
	v_min_u32_e32 v16, s35, v9

.Lw1b50:
	v_lshl_add_u32 v16, v16, 2, s34
	ds_read_b32 v16, v16
	v_add_u32_e32 v10, 8, v46
	v_min_u32_e32 v17, s35, v10
	v_lshl_add_u32 v17, v17, 2, s34
	ds_read_b32 v17, v17
	v_add_u32_e32 v19, 8, v47
	v_min_u32_e32 v18, s35, v19
	v_lshl_add_u32 v18, v18, 2, s34
	ds_read_b32 v18, v18

.Lw1b51:
	s_waitcnt lgkmcnt(7)
	v_cmp_le_i32_e64 s[36:37], v11, v32
	s_waitcnt lgkmcnt(6)
	v_cmp_le_i32_e64 s[38:39], v12, v33
	s_waitcnt lgkmcnt(5)
	v_cmp_le_i32_e64 s[58:59], v13, v34
	s_waitcnt lgkmcnt(4)
	v_cmp_le_i32_e64 s[60:61], v14, v35
	v_cndmask_b32_e64 v40, v40, v3, s[36:37]

.Lw1b52:
	v_cndmask_b32_e64 v41, v41, v4, s[38:39]
	v_cndmask_b32_e64 v42, v42, v6, s[58:59]
	v_cndmask_b32_e64 v43, v43, v7, s[60:61]
	s_waitcnt lgkmcnt(3)
	v_cmp_le_i32_e64 s[36:37], v15, v36
	s_waitcnt lgkmcnt(2)
	v_cmp_le_i32_e64 s[38:39], v16, v37
	s_waitcnt lgkmcnt(1)
	v_cmp_le_i32_e64 s[58:59], v17, v38

.Lw1b53:
	s_waitcnt lgkmcnt(0)
	v_cmp_le_i32_e64 s[60:61], v18, v39
	v_cndmask_b32_e64 v44, v44, v8, s[36:37]
	v_cndmask_b32_e64 v45, v45, v9, s[38:39]
	v_cndmask_b32_e64 v46, v46, v10, s[58:59]
	v_cndmask_b32_e64 v47, v47, v19, s[60:61]
	v_add_u32_e32 v3, 4, v40
	v_min_u32_e32 v11, s35, v3
	v_lshl_add_u32 v11, v11, 2, s34

.Lw1b54:
	ds_read_b32 v11, v11
	v_add_u32_e32 v4, 4, v41
	v_min_u32_e32 v12, s35, v4
	v_lshl_add_u32 v12, v12, 2, s34
	ds_read_b32 v12, v12
	v_add_u32_e32 v6, 4, v42
	v_min_u32_e32 v13, s35, v6
	v_lshl_add_u32 v13, v13, 2, s34
	ds_read_b32 v13, v13
	v_add_u32_e32 v7, 4, v43

.Lw1b55:
	v_min_u32_e32 v14, s35, v7
	v_lshl_add_u32 v14, v14, 2, s34
	ds_read_b32 v14, v14
	v_add_u32_e32 v8, 4, v44
	v_min_u32_e32 v15, s35, v8
	v_lshl_add_u32 v15, v15, 2, s34
	ds_read_b32 v15, v15
	v_add_u32_e32 v9, 4, v45
	v_min_u32_e32 v16, s35, v9
	v_lshl_add_u32 v16, v16, 2, s34

.Lw1b56:
	ds_read_b32 v16, v16
	v_add_u32_e32 v10, 4, v46
	v_min_u32_e32 v17, s35, v10
	v_lshl_add_u32 v17, v17, 2, s34
	ds_read_b32 v17, v17
	v_add_u32_e32 v19, 4, v47
	v_min_u32_e32 v18, s35, v19
	v_lshl_add_u32 v18, v18, 2, s34
	ds_read_b32 v18, v18
	s_waitcnt lgkmcnt(7)

.Lw1b57:
	v_cmp_le_i32_e64 s[36:37], v11, v32
	s_waitcnt lgkmcnt(6)
	v_cmp_le_i32_e64 s[38:39], v12, v33
	s_waitcnt lgkmcnt(5)
	v_cmp_le_i32_e64 s[58:59], v13, v34
	s_waitcnt lgkmcnt(4)
	v_cmp_le_i32_e64 s[60:61], v14, v35
	v_cndmask_b32_e64 v40, v40, v3, s[36:37]
	v_cndmask_b32_e64 v41, v41, v4, s[38:39]

.Lw1b58:
	v_cndmask_b32_e64 v42, v42, v6, s[58:59]
	v_cndmask_b32_e64 v43, v43, v7, s[60:61]
	s_waitcnt lgkmcnt(3)
	v_cmp_le_i32_e64 s[36:37], v15, v36
	s_waitcnt lgkmcnt(2)
	v_cmp_le_i32_e64 s[38:39], v16, v37
	s_waitcnt lgkmcnt(1)
	v_cmp_le_i32_e64 s[58:59], v17, v38
	s_waitcnt lgkmcnt(0)
	v_cmp_le_i32_e64 s[60:61], v18, v39

.Lw1b59:
	v_cndmask_b32_e64 v44, v44, v8, s[36:37]
	v_cndmask_b32_e64 v45, v45, v9, s[38:39]
	v_cndmask_b32_e64 v46, v46, v10, s[58:59]
	v_cndmask_b32_e64 v47, v47, v19, s[60:61]
	v_add_u32_e32 v3, 2, v40
	v_min_u32_e32 v11, s35, v3
	v_lshl_add_u32 v11, v11, 2, s34
	ds_read_b32 v11, v11

.Lw1b60:
	v_add_u32_e32 v4, 2, v41
	v_min_u32_e32 v12, s35, v4
	v_lshl_add_u32 v12, v12, 2, s34
	ds_read_b32 v12, v12
	v_add_u32_e32 v6, 2, v42
	v_min_u32_e32 v13, s35, v6
	v_lshl_add_u32 v13, v13, 2, s34
	ds_read_b32 v13, v13
	v_add_u32_e32 v7, 2, v43
	v_min_u32_e32 v14, s35, v7
	v_lshl_add_u32 v14, v14, 2, s34

.Lw1b61:
	ds_read_b32 v14, v14
	v_add_u32_e32 v8, 2, v44
	v_min_u32_e32 v15, s35, v8
	v_lshl_add_u32 v15, v15, 2, s34
	ds_read_b32 v15, v15
	v_add_u32_e32 v9, 2, v45
	v_min_u32_e32 v16, s35, v9
	v_lshl_add_u32 v16, v16, 2, s34
	ds_read_b32 v16, v16

.Lw1b62:
	v_add_u32_e32 v10, 2, v46
	v_min_u32_e32 v17, s35, v10
	v_lshl_add_u32 v17, v17, 2, s34
	ds_read_b32 v17, v17
	v_add_u32_e32 v19, 2, v47
	v_min_u32_e32 v18, s35, v19
	v_lshl_add_u32 v18, v18, 2, s34
	ds_read_b32 v18, v18
	s_waitcnt lgkmcnt(7)
	v_cmp_le_i32_e64 s[36:37], v11, v32

.Lw1b63:
	s_waitcnt lgkmcnt(6)
	v_cmp_le_i32_e64 s[38:39], v12, v33
	s_waitcnt lgkmcnt(5)
	v_cmp_le_i32_e64 s[58:59], v13, v34
	s_waitcnt lgkmcnt(4)
	v_cmp_le_i32_e64 s[60:61], v14, v35
	v_cndmask_b32_e64 v40, v40, v3, s[36:37]
	v_cndmask_b32_e64 v41, v41, v4, s[38:39]
	v_cndmask_b32_e64 v42, v42, v6, s[58:59]

.Lw1b64:
	v_cndmask_b32_e64 v43, v43, v7, s[60:61]
	s_waitcnt lgkmcnt(3)
	v_cmp_le_i32_e64 s[36:37], v15, v36
	s_waitcnt lgkmcnt(2)
	v_cmp_le_i32_e64 s[38:39], v16, v37
	s_waitcnt lgkmcnt(1)
	v_cmp_le_i32_e64 s[58:59], v17, v38
	s_waitcnt lgkmcnt(0)
	v_cmp_le_i32_e64 s[60:61], v18, v39
	v_cndmask_b32_e64 v44, v44, v8, s[36:37]

.Lw1b65:
	v_cndmask_b32_e64 v45, v45, v9, s[38:39]
	v_cndmask_b32_e64 v46, v46, v10, s[58:59]
	v_cndmask_b32_e64 v47, v47, v19, s[60:61]
	v_add_u32_e32 v3, 1, v40
	v_min_u32_e32 v11, s35, v3
	v_lshl_add_u32 v11, v11, 2, s34
	ds_read_b32 v11, v11
	v_add_u32_e32 v4, 1, v41
	v_min_u32_e32 v12, s35, v4

.Lw1b66:
	v_lshl_add_u32 v12, v12, 2, s34
	ds_read_b32 v12, v12
	v_add_u32_e32 v6, 1, v42
	v_min_u32_e32 v13, s35, v6
	v_lshl_add_u32 v13, v13, 2, s34
	ds_read_b32 v13, v13
	v_add_u32_e32 v7, 1, v43
	v_min_u32_e32 v14, s35, v7
	v_lshl_add_u32 v14, v14, 2, s34
	ds_read_b32 v14, v14

.Lw1b67:
	v_add_u32_e32 v8, 1, v44
	v_min_u32_e32 v15, s35, v8
	v_lshl_add_u32 v15, v15, 2, s34
	ds_read_b32 v15, v15
	v_add_u32_e32 v9, 1, v45
	v_min_u32_e32 v16, s35, v9
	v_lshl_add_u32 v16, v16, 2, s34
	ds_read_b32 v16, v16
	v_add_u32_e32 v10, 1, v46
	v_min_u32_e32 v17, s35, v10

.Lw1b68:
	v_lshl_add_u32 v17, v17, 2, s34
	ds_read_b32 v17, v17
	v_add_u32_e32 v19, 1, v47
	v_min_u32_e32 v18, s35, v19
	v_lshl_add_u32 v18, v18, 2, s34
	ds_read_b32 v18, v18
	s_waitcnt lgkmcnt(7)
	v_cmp_le_i32_e64 s[36:37], v11, v32
	s_waitcnt lgkmcnt(6)
	v_cmp_le_i32_e64 s[38:39], v12, v33

.Lw1b69:
	s_waitcnt lgkmcnt(5)
	v_cmp_le_i32_e64 s[58:59], v13, v34
	s_waitcnt lgkmcnt(4)
	v_cmp_le_i32_e64 s[60:61], v14, v35
	v_cndmask_b32_e64 v40, v40, v3, s[36:37]
	v_cndmask_b32_e64 v41, v41, v4, s[38:39]
	v_cndmask_b32_e64 v42, v42, v6, s[58:59]
	v_cndmask_b32_e64 v43, v43, v7, s[60:61]

.Lw1b70:
	s_waitcnt lgkmcnt(3)
	v_cmp_le_i32_e64 s[36:37], v15, v36
	s_waitcnt lgkmcnt(2)
	v_cmp_le_i32_e64 s[38:39], v16, v37
	s_waitcnt lgkmcnt(1)
	v_cmp_le_i32_e64 s[58:59], v17, v38
	s_waitcnt lgkmcnt(0)
	v_cmp_le_i32_e64 s[60:61], v18, v39
	v_cndmask_b32_e64 v44, v44, v8, s[36:37]
	v_cndmask_b32_e64 v45, v45, v9, s[38:39]

.Lw1b71:
	v_cndmask_b32_e64 v46, v46, v10, s[58:59]
	v_cndmask_b32_e64 v47, v47, v19, s[60:61]
	v_lshl_add_u32 v11, v40, 2, s34
	ds_read_b32 v3, v11
	ds_read_b32 v11, v11 offset:400
	v_lshl_add_u32 v12, v41, 2, s34
	ds_read_b32 v4, v12

.Lw1b72:
	ds_read_b32 v12, v12 offset:400
	v_lshl_add_u32 v13, v42, 2, s34
	ds_read_b32 v6, v13
	ds_read_b32 v13, v13 offset:400
	v_lshl_add_u32 v14, v43, 2, s34
	ds_read_b32 v7, v14
	ds_read_b32 v14, v14 offset:400
	v_lshl_add_u32 v15, v44, 2, s34

.Lw1b73:
	ds_read_b32 v8, v15
	ds_read_b32 v15, v15 offset:400
	v_lshl_add_u32 v16, v45, 2, s34
	ds_read_b32 v9, v16
	ds_read_b32 v16, v16 offset:400
	v_lshl_add_u32 v17, v46, 2, s34
	ds_read_b32 v10, v17

.Lw1b74:
	ds_read_b32 v17, v17 offset:400
	v_lshl_add_u32 v18, v47, 2, s34
	ds_read_b32 v19, v18
	ds_read_b32 v18, v18 offset:400
	s_waitcnt lgkmcnt(14)
	v_sub_u32_e32 v3, v32, v3
	v_lshl_add_u32 v40, v40, 13, v3
	v_add_lshl_u32 v40, v40, v11, 2
	s_waitcnt lgkmcnt(12)

.Lw1b75:
	v_sub_u32_e32 v4, v33, v4
	v_lshl_add_u32 v41, v41, 13, v4
	v_add_lshl_u32 v41, v41, v12, 2
	s_waitcnt lgkmcnt(10)
	v_sub_u32_e32 v6, v34, v6
	v_lshl_add_u32 v42, v42, 13, v6
	v_add_lshl_u32 v42, v42, v13, 2
	s_waitcnt lgkmcnt(8)
	v_sub_u32_e32 v7, v35, v7
	v_lshl_add_u32 v43, v43, 13, v7

.Lw1b76:
	v_add_lshl_u32 v43, v43, v14, 2
	s_waitcnt lgkmcnt(6)
	v_sub_u32_e32 v8, v36, v8
	v_lshl_add_u32 v44, v44, 13, v8
	v_add_lshl_u32 v44, v44, v15, 2
	s_waitcnt lgkmcnt(4)
	v_sub_u32_e32 v9, v37, v9
	v_lshl_add_u32 v45, v45, 13, v9
	v_add_lshl_u32 v45, v45, v16, 2
	s_waitcnt lgkmcnt(2)

.Lw1b77:
	v_sub_u32_e32 v10, v38, v10
	v_lshl_add_u32 v46, v46, 13, v10
	v_add_lshl_u32 v46, v46, v17, 2
	s_waitcnt lgkmcnt(0)
	v_sub_u32_e32 v19, v39, v19
	v_lshl_add_u32 v47, v47, 13, v19
	v_add_lshl_u32 v47, v47, v18, 2
	v_cmp_gt_i32_e64 s[36:37], s3, v32
	v_mov_b32_e32 v3, -1
	s_mov_b64 exec, s[36:37]

.Lw1b78:
	global_load_dword v3, v40, s[28:29]
	s_mov_b64 exec, -1
	v_cmp_gt_i32_e64 s[38:39], s3, v33
	v_mov_b32_e32 v4, -1
	s_mov_b64 exec, s[38:39]
	global_load_dword v4, v41, s[28:29]
	s_mov_b64 exec, -1
	v_cmp_gt_i32_e64 s[58:59], s3, v34
	v_mov_b32_e32 v6, -1
	s_mov_b64 exec, s[58:59]
	global_load_dword v6, v42, s[28:29]

.Lw1b79:
	s_mov_b64 exec, -1
	v_cmp_gt_i32_e64 s[60:61], s3, v35
	v_mov_b32_e32 v7, -1
	s_mov_b64 exec, s[60:61]
	global_load_dword v7, v43, s[28:29]
	s_mov_b64 exec, -1
	v_cmp_gt_i32_e64 s[36:37], s3, v36
	v_mov_b32_e32 v8, -1
	s_mov_b64 exec, s[36:37]
	global_load_dword v8, v44, s[28:29]

.Lw1b80:
	s_mov_b64 exec, -1
	v_cmp_gt_i32_e64 s[38:39], s3, v37
	v_mov_b32_e32 v9, -1
	s_mov_b64 exec, s[38:39]
	global_load_dword v9, v45, s[28:29]
	s_mov_b64 exec, -1
	v_cmp_gt_i32_e64 s[58:59], s3, v38
	v_mov_b32_e32 v10, -1
	s_mov_b64 exec, s[58:59]
	global_load_dword v10, v46, s[28:29]
	s_mov_b64 exec, -1

.Lw1b81:
	v_cmp_gt_i32_e64 s[60:61], s3, v39
	v_mov_b32_e32 v13, -1
	s_mov_b64 exec, s[60:61]
	global_load_dword v13, v47, s[28:29]
	s_mov_b64 exec, -1
	v_mov_b32_e32 v19, 1
	s_waitcnt vmcnt(7)
	v_cmp_ne_u32_e64 s[36:37], -1, v3
	v_lshrrev_b32_e32 v32, 15, v3
	v_and_b32_e32 v32, 0x1fffc, v32
	v_add_u32_e32 v32, 0x10000, v32

.Lw1b82:
	v_mov_b32_e32 v15, 0
	s_mov_b64 exec, s[36:37]
	ds_add_rtn_u32 v15, v32, v19
	s_mov_b64 exec, -1
	s_waitcnt vmcnt(6)
	v_cmp_ne_u32_e64 s[38:39], -1, v4
	v_lshrrev_b32_e32 v33, 15, v4
	v_and_b32_e32 v33, 0x1fffc, v33
	v_add_u32_e32 v33, 0x10000, v33
	v_mov_b32_e32 v5, 0

.Lw1b83:
	s_mov_b64 exec, s[38:39]
	ds_add_rtn_u32 v5, v33, v19
	s_mov_b64 exec, -1
	s_waitcnt vmcnt(5)
	v_cmp_ne_u32_e64 s[58:59], -1, v6
	v_lshrrev_b32_e32 v34, 15, v6
	v_and_b32_e32 v34, 0x1fffc, v34
	v_add_u32_e32 v34, 0x10000, v34
	v_mov_b32_e32 v16, 0
	s_mov_b64 exec, s[58:59]
	ds_add_rtn_u32 v16, v34, v19

.Lw1b84:
	s_mov_b64 exec, -1
	s_waitcnt vmcnt(4)
	v_cmp_ne_u32_e64 s[60:61], -1, v7
	v_lshrrev_b32_e32 v35, 15, v7
	v_and_b32_e32 v35, 0x1fffc, v35
	v_add_u32_e32 v35, 0x10000, v35
	v_mov_b32_e32 v11, 0
	s_mov_b64 exec, s[60:61]
	ds_add_rtn_u32 v11, v35, v19
	s_mov_b64 exec, -1

.Lw1b85:
	s_waitcnt vmcnt(3)
	v_cmp_ne_u32_e64 s[36:37], -1, v8
	v_lshrrev_b32_e32 v36, 15, v8
	v_and_b32_e32 v36, 0x1fffc, v36
	v_add_u32_e32 v36, 0x10000, v36
	v_mov_b32_e32 v17, 0
	s_mov_b64 exec, s[36:37]
	ds_add_rtn_u32 v17, v36, v19
	s_mov_b64 exec, -1
	s_waitcnt vmcnt(2)
	v_cmp_ne_u32_e64 s[38:39], -1, v9

.Lw1b86:
	v_lshrrev_b32_e32 v37, 15, v9
	v_and_b32_e32 v37, 0x1fffc, v37
	v_add_u32_e32 v37, 0x10000, v37
	v_mov_b32_e32 v12, 0
	s_mov_b64 exec, s[38:39]
	ds_add_rtn_u32 v12, v37, v19
	s_mov_b64 exec, -1
	s_waitcnt vmcnt(1)
	v_cmp_ne_u32_e64 s[58:59], -1, v10
	v_lshrrev_b32_e32 v38, 15, v10

.Lw1b87:
	v_and_b32_e32 v38, 0x1fffc, v38
	v_add_u32_e32 v38, 0x10000, v38
	v_mov_b32_e32 v18, 0
	s_mov_b64 exec, s[58:59]
	ds_add_rtn_u32 v18, v38, v19
	s_mov_b64 exec, -1
	s_waitcnt vmcnt(0)
	v_cmp_ne_u32_e64 s[60:61], -1, v13
	v_lshrrev_b32_e32 v39, 15, v13
	v_and_b32_e32 v39, 0x1fffc, v39

.Lw1b88:
	v_add_u32_e32 v39, 0x10000, v39
	v_mov_b32_e32 v14, 0
	s_mov_b64 exec, s[60:61]
	ds_add_rtn_u32 v14, v39, v19
	s_mov_b64 exec, -1
	s_branch .LBB1_232
.LBB1_231:
	v_mov_b32_e32 v13, 0
	v_mov_b32_e32 v10, 0
	v_mov_b32_e32 v9, 0
	v_mov_b32_e32 v8, 0
	v_mov_b32_e32 v7, 0
	v_mov_b32_e32 v6, 0
	v_mov_b32_e32 v4, 0
.Lw1t89:
	s_cbranch_execz .Lw1c89
.Lw1b89:
	v_mov_b32_e32 v3, 0
.LBB1_232:
	v_cmp_lt_i32_e32 vcc, s57, v2
	v_mov_b32_e32 v2, 0
	s_waitcnt lgkmcnt(0)
	s_barrier
	s_and_saveexec_b64 s[34:35], s[22:23]
	v_mov_b32_e32 v2, 0x10000
	v_lshl_or_b32 v2, v0, 2, v2
	ds_read_b32 v2, v2
	s_or_b64 exec, exec, s[34:35]
	s_waitcnt lgkmcnt(0)
	v_add_u32_dpp v19, v2, v2 row_shr:1 row_mask:0xf bank_mask:0xf bound_ctrl:1

.Lw1b90:
	s_nop 1
	v_add_u32_dpp v19, v19, v19 row_shr:2 row_mask:0xf bank_mask:0xf bound_ctrl:1
	s_nop 1
	v_add_u32_dpp v19, v19, v19 row_shr:4 row_mask:0xf bank_mask:0xf bound_ctrl:1
	s_nop 1
	v_add_u32_dpp v19, v19, v19 row_shr:8 row_mask:0xf bank_mask:0xf bound_ctrl:1
	s_nop 1
	v_add_u32_dpp v19, v19, v19 row_bcast:15 row_mask:0xa bank_mask:0xf
	s_nop 1
	v_add_u32_dpp v19, v19, v19 row_bcast:31 row_mask:0xc bank_mask:0xf

.Lw1b91:
	s_and_saveexec_b64 s[34:35], s[4:5]
	v_mov_b32_e32 v20, 0x11b60
	v_lshl_add_u32 v1, v1, 2, v20
	ds_write_b32 v1, v19
	s_or_b64 exec, exec, s[34:35]
	s_add_i32 s41, s41, s40
	s_add_i32 s42, s42, s41
	s_add_i32 s43, s43, s42
	s_add_i32 s44, s44, s43
	s_add_i32 s45, s45, s44
	s_add_i32 s46, s46, s45

.Lw1b92:
	s_add_i32 s47, s47, s46
	s_add_i32 s48, s48, s47
	s_add_i32 s49, s49, s48
	s_add_i32 s50, s50, s49
	s_add_i32 s51, s51, s50
	s_add_i32 s52, s52, s51
	s_add_i32 s53, s53, s52
	s_add_i32 s54, s54, s53
	s_add_i32 s34, s55, s54
	s_waitcnt lgkmcnt(0)
	s_barrier
	s_and_saveexec_b64 s[36:37], s[22:23]
	s_cbranch_execz .LBB1_239
	v_mov_b32_e32 v1, 0x11b98

.Lw1b93:
	v_mov_b32_e32 v20, 0x11b70
	ds_read_b32 v1, v1
	ds_read_b96 v[24:26], v20
	v_mov_b32_e32 v20, 0x11b60
	ds_read_b128 v[20:23], v20
	v_sub_u32_e32 v2, v19, v2
	s_waitcnt lgkmcnt(2)
	v_cndmask_b32_e64 v1, 0, v1, s[20:21]
	s_waitcnt lgkmcnt(1)

.Lw1b94:
	v_cndmask_b32_e64 v24, 0, v24, s[14:15]
	v_cndmask_b32_e64 v26, 0, v26, s[18:19]
	s_waitcnt lgkmcnt(0)
	v_cndmask_b32_e64 v22, 0, v22, s[10:11]
	v_cndmask_b32_e64 v21, 0, v21, s[8:9]
	v_cndmask_b32_e64 v20, v20, 0, s[6:7]
	v_cndmask_b32_e64 v23, 0, v23, s[12:13]
	v_add3_u32 v20, v21, v20, v22

.Lw1b95:
	v_cndmask_b32_e64 v25, 0, v25, s[16:17]
	v_add3_u32 v20, v23, v20, v24
	v_add3_u32 v20, v25, v20, v26
	v_add3_u32 v1, v1, v20, v2
	v_mov_b32_e32 v2, 0x11000
	v_lshl_or_b32 v2, v0, 2, v2
	ds_write_b32 v2, v1
	v_lshl_or_b32 v2, s33, 9, v0

.Lw1b96:
	s_mov_b32 s4, 0x186a0
	v_cmp_gt_u32_e64 s[4:5], s4, v2
	s_and_b64 exec, exec, s[4:5]
	s_cbranch_execz .LBB1_239
	s_and_b64 s[4:5], s[30:31], exec
	s_cselect_b32 s4, 0x186a1, 0
	v_add_u32_e32 v20, s4, v2
	v_mov_b32_e32 v21, 0
	v_lshl_add_u64 v[20:21], v[20:21], 2, s[24:25]
	v_add_u32_e32 v1, s34, v1

.Lw1b97:
	global_store_dword v[20:21], v1, off
.LBB1_239:
	s_or_b64 exec, exec, s[36:37]
	s_cmpk_eq_i32 s33, 0xc3
	s_cselect_b64 s[6:7], -1, 0
	v_cmp_eq_u32_e64 s[4:5], 0, v0
	s_and_b64 s[6:7], s[4:5], s[6:7]
	s_and_saveexec_b64 s[4:5], s[6:7]
	s_cbranch_execz .LBB1_241
	s_and_b64 s[6:7], s[30:31], exec
	s_cselect_b32 s6, 0x61a84, 0
	s_add_u32 s6, s24, s6
	s_addc_u32 s7, s25, 0

.Lw1b98:
	v_mov_b32_e32 v1, 0x61000
	v_mov_b32_e32 v2, 0xc3500
	global_store_dword v1, v2, s[6:7] offset:2688
.LBB1_241:
	s_or_b64 exec, exec, s[4:5]
	s_add_u32 s6, s26, s56
	s_addc_u32 s7, s27, 0
	s_ashr_i32 s35, s34, 31
	s_lshl_b64 s[4:5], s[34:35], 2
	s_add_u32 s8, s6, s4
	s_addc_u32 s9, s7, s5
	s_mov_b64 s[4:5], -1
	s_and_b64 vcc, exec, vcc
.Lw1t99:
	s_cbranch_execz .Lw1c99
.Lw1b99:
	s_waitcnt lgkmcnt(0)
	s_barrier
	s_cbranch_vccz .LBB1_265
	v_mov_b32_e32 v1, 0x11900
	ds_read_b32 v1, v1
	s_mov_b64 s[4:5], 0
	v_mov_b32_e32 v2, 0x11880
	s_movk_i32 s12, 0x51
	s_movk_i32 s13, 0x52
	s_movk_i32 s14, 0x59
	s_movk_i32 s15, 0x5a
	s_movk_i32 s16, 0x5d

.Lw1b100:
	s_movk_i32 s17, 0x5e
	s_movk_i32 s18, 0x5f
	s_movk_i32 s19, 0x60
	s_movk_i32 s20, 0x61
	v_mov_b32_e32 v19, 0x11990
	v_mov_b32_e32 v20, 1
	v_mov_b32_e32 v21, 0x11840
	v_mov_b32_e32 v22, 0x11820
	v_mov_b32_e32 v23, 0x11810
	v_mov_b32_e32 v24, 0x11808

.Lw1b101:
	v_mov_b32_e32 v25, 0x11804
	v_mov_b32_e32 v26, 0x11800
	v_mov_b32_e32 v27, v0
	s_branch .LBB1_244
.LBB1_243:
	s_or_b64 exec, exec, s[10:11]
	v_lshl_add_u32 v28, v30, 2, v19
	ds_read_b32 v28, v28
	s_waitcnt lgkmcnt(0)
	v_lshl_add_u32 v28, v30, 13, v28
	v_sub_u32_e32 v28, v28, v29
.Lw1t102:
	s_cbranch_execz .Lw1c102
.Lw1b102:
	v_add_u32_e32 v28, v27, v28
	v_ashrrev_i32_e32 v29, 31, v28
	v_lshl_add_u64 v[28:29], v[28:29], 2, s[28:29]
	global_load_dword v28, v[28:29], off
	v_add_u32_e32 v27, 0x400, v27
	v_cmp_le_i32_e32 vcc, s3, v27
	s_or_b64 s[4:5], vcc, s[4:5]
	s_waitcnt vmcnt(0)
	v_lshrrev_b32_e32 v29, 15, v28
	v_and_b32_e32 v29, 0x1fffc, v29
	v_add_u32_e32 v30, 0x11000, v29

.Lw1b103:
	v_add_u32_e32 v29, 0x10800, v29
	ds_read_b32 v30, v30
	ds_add_rtn_u32 v29, v29, v20
	v_and_b32_e32 v31, 0x1fffff, v28
	s_waitcnt lgkmcnt(0)
	v_add_u32_e32 v28, v29, v30
	v_ashrrev_i32_e32 v29, 31, v28
	v_lshl_add_u64 v[28:29], v[28:29], 2, s[8:9]
	global_store_dword v[28:29], v31, off

.Lw1b104:
	s_andn2_b64 exec, exec, s[4:5]
	s_cbranch_execz .LBB1_264
.LBB1_244:
	s_waitcnt lgkmcnt(0)
	v_cmp_gt_i32_e32 vcc, v1, v27
	s_nop 1
	v_cndmask_b32_e64 v28, 64, 0, vcc
	v_lshl_or_b32 v29, v28, 2, v2
	ds_read_b32 v29, v29
	v_or_b32_e32 v30, 32, v28
	s_waitcnt lgkmcnt(0)
	v_cmp_gt_i32_e32 vcc, v29, v27

.Lw1b105:
	s_nop 1
	v_cndmask_b32_e32 v29, v30, v28, vcc
	v_cmp_lt_u32_e64 s[6:7], s12, v29
	v_cmp_gt_u32_e32 vcc, s13, v29
	s_and_saveexec_b64 s[10:11], vcc
	s_cbranch_execz .LBB1_246
	v_lshl_add_u32 v28, v29, 2, v21
	ds_read_b32 v30, v28
	s_andn2_b64 s[6:7], s[6:7], exec
	v_or_b32_e32 v28, 16, v29
	s_waitcnt lgkmcnt(0)
	v_cmp_gt_i32_e32 vcc, v30, v27

.LBB1_246:
	s_or_b64 exec, exec, s[10:11]
	s_and_saveexec_b64 s[10:11], s[6:7]
	v_mov_b32_e32 v28, v29
	s_or_b64 exec, exec, s[10:11]
	v_cmp_lt_u32_e64 s[6:7], s14, v28
	v_cmp_gt_u32_e32 vcc, s15, v28
	s_and_saveexec_b64 s[10:11], vcc
	s_cbranch_execz .LBB1_250
	v_lshl_add_u32 v29, v28, 2, v22
	ds_read_b32 v30, v29

.Lw1b107:
	s_andn2_b64 s[6:7], s[6:7], exec
	v_add_u32_e32 v29, 8, v28
	s_waitcnt lgkmcnt(0)
	v_cmp_gt_i32_e32 vcc, v30, v27
	s_and_b64 s[22:23], vcc, exec
	s_or_b64 s[6:7], s[6:7], s[22:23]
.LBB1_250:
	s_or_b64 exec, exec, s[10:11]
	s_and_saveexec_b64 s[10:11], s[6:7]
	v_mov_b32_e32 v29, v28
	s_or_b64 exec, exec, s[10:11]
	v_cmp_lt_u32_e64 s[6:7], s16, v29
	v_cmp_gt_u32_e32 vcc, s17, v29
	s_and_saveexec_b64 s[10:11], vcc
	s_cbranch_execz .LBB1_254
.Lw1t108:
	s_cbranch_execz .Lw1c108
.Lw1b108:
	v_lshl_add_u32 v28, v29, 2, v23
	ds_read_b32 v28, v28
	s_andn2_b64 s[6:7], s[6:7], exec
	v_add_u32_e32 v30, 4, v29
	s_waitcnt lgkmcnt(0)
	v_cmp_gt_i32_e32 vcc, v28, v27
	s_and_b64 s[22:23], vcc, exec
	s_or_b64 s[6:7], s[6:7], s[22:23]
.LBB1_254:
	s_or_b64 exec, exec, s[10:11]
	s_and_saveexec_b64 s[10:11], s[6:7]
	v_mov_b32_e32 v30, v29
	s_or_b64 exec, exec, s[10:11]
	v_cmp_lt_u32_e64 s[6:7], s18, v30
.Lw1t109:
	s_cbranch_execz .Lw1c109
.Lw1b109:
	v_cmp_gt_u32_e32 vcc, s19, v30
	s_and_saveexec_b64 s[10:11], vcc
	s_cbranch_execz .LBB1_258
	v_lshl_add_u32 v28, v30, 2, v24
	ds_read_b32 v29, v28
	s_andn2_b64 s[6:7], s[6:7], exec
	v_add_u32_e32 v28, 2, v30
	s_waitcnt lgkmcnt(0)
	v_cmp_gt_i32_e32 vcc, v29, v27
	s_and_b64 s[22:23], vcc, exec
	s_or_b64 s[6:7], s[6:7], s[22:23]

.Lw1b110:
	s_and_saveexec_b64 s[10:11], s[6:7]
	v_mov_b32_e32 v28, v30
	s_or_b64 exec, exec, s[10:11]
	v_cmp_lt_u32_e64 s[6:7], s19, v28
	v_cmp_gt_u32_e32 vcc, s20, v28
	s_and_saveexec_b64 s[10:11], vcc
	s_cbranch_execz .LBB1_262
	v_lshl_add_u32 v29, v28, 2, v25
	ds_read_b32 v29, v29
	s_andn2_b64 s[6:7], s[6:7], exec
	v_add_u32_e32 v30, 1, v28
	s_waitcnt lgkmcnt(0)

.Lw1b111:
	v_cmp_gt_i32_e32 vcc, v29, v27
	s_and_b64 s[22:23], vcc, exec
	s_or_b64 s[6:7], s[6:7], s[22:23]

.LBB1_265:
	s_and_b64 vcc, exec, s[4:5]
.Lw1t112:
	s_cbranch_execz .Lw1c112
.Lw1b112:
	s_cbranch_vccz .LBB1_390
	v_cmp_ne_u32_e32 vcc, -1, v3
	s_and_saveexec_b64 s[4:5], vcc
	s_cbranch_execz .LBB1_274
	v_lshrrev_b32_e32 v1, 15, v3
	v_and_b32_e32 v1, 0x1fffc, v1
	v_add_u32_e32 v1, 0x11000, v1
	ds_read_b32 v1, v1
	v_lshlrev_b32_e32 v2, 2, v15
	s_waitcnt lgkmcnt(0)
	v_lshl_add_u32 v1, v1, 2, v2

.Lw1b113:
	ds_write_b32 v1, v3
	s_or_b64 exec, exec, s[4:5]
	v_cmp_ne_u32_e32 vcc, -1, v4
	s_and_saveexec_b64 s[4:5], vcc
	s_cbranch_execnz .LBB1_275

.LBB1_269:
	v_lshrrev_b32_e32 v1, 15, v6
	v_and_b32_e32 v1, 0x1fffc, v1
	v_add_u32_e32 v1, 0x11000, v1
.Lw1t114:
	s_cbranch_execz .Lw1c114
.Lw1b114:
	ds_read_b32 v1, v1
	v_lshlrev_b32_e32 v2, 2, v16
	s_waitcnt lgkmcnt(0)
	v_lshl_add_u32 v1, v1, 2, v2
	ds_write_b32 v1, v6
	s_or_b64 exec, exec, s[4:5]
	v_cmp_ne_u32_e32 vcc, -1, v7
	s_and_saveexec_b64 s[4:5], vcc
	s_cbranch_execnz .LBB1_277
.LBB1_270:
	s_or_b64 exec, exec, s[4:5]
	v_cmp_ne_u32_e32 vcc, -1, v8
	s_and_saveexec_b64 s[4:5], vcc
.Lw1t115:
	s_cbranch_execz .Lw1c115

.LBB1_271:
	v_lshrrev_b32_e32 v1, 15, v8
	v_and_b32_e32 v1, 0x1fffc, v1
	v_add_u32_e32 v1, 0x11000, v1
	ds_read_b32 v1, v1
	v_lshlrev_b32_e32 v2, 2, v17
	s_waitcnt lgkmcnt(0)
	v_lshl_add_u32 v1, v1, 2, v2
	ds_write_b32 v1, v8
	s_or_b64 exec, exec, s[4:5]

.Lw1b116:
	v_cmp_ne_u32_e32 vcc, -1, v9
	s_and_saveexec_b64 s[4:5], vcc
	s_cbranch_execnz .LBB1_279

.LBB1_273:
	v_lshrrev_b32_e32 v1, 15, v10
	v_and_b32_e32 v1, 0x1fffc, v1
	v_add_u32_e32 v1, 0x11000, v1
	ds_read_b32 v1, v1
	v_lshlrev_b32_e32 v2, 2, v18
.Lw1t117:
	s_cbranch_execz .Lw1c117
.Lw1b117:
	s_waitcnt lgkmcnt(0)
	v_lshl_add_u32 v1, v1, 2, v2
	ds_write_b32 v1, v10
	s_or_b64 exec, exec, s[4:5]
	v_cmp_ne_u32_e32 vcc, -1, v13
	s_and_saveexec_b64 s[4:5], vcc
	s_cbranch_execnz .LBB1_281
	s_branch .LBB1_282

.LBB1_275:
	v_lshrrev_b32_e32 v1, 15, v4
.Lw1t118:
	s_cbranch_execz .Lw1c118
.Lw1b118:
	v_and_b32_e32 v1, 0x1fffc, v1
	v_add_u32_e32 v1, 0x11000, v1
	ds_read_b32 v1, v1
	v_lshlrev_b32_e32 v2, 2, v5
	s_waitcnt lgkmcnt(0)
	v_lshl_add_u32 v1, v1, 2, v2
	ds_write_b32 v1, v4
	s_or_b64 exec, exec, s[4:5]
	v_cmp_ne_u32_e32 vcc, -1, v6
	s_and_saveexec_b64 s[4:5], vcc

.LBB1_277:
	v_lshrrev_b32_e32 v1, 15, v7
	v_and_b32_e32 v1, 0x1fffc, v1
	v_add_u32_e32 v1, 0x11000, v1
	ds_read_b32 v1, v1
	v_lshlrev_b32_e32 v2, 2, v11
	s_waitcnt lgkmcnt(0)
	v_lshl_add_u32 v1, v1, 2, v2
.Lw1t120:
	s_cbranch_execz .Lw1c120
.Lw1b120:
	ds_write_b32 v1, v7
	s_or_b64 exec, exec, s[4:5]
	v_cmp_ne_u32_e32 vcc, -1, v8
	s_and_saveexec_b64 s[4:5], vcc
	s_cbranch_execnz .LBB1_271

.LBB1_279:
	v_lshrrev_b32_e32 v1, 15, v9
	v_and_b32_e32 v1, 0x1fffc, v1
	v_add_u32_e32 v1, 0x11000, v1
.Lw1t121:
	s_cbranch_execz .Lw1c121
.Lw1b121:
	ds_read_b32 v1, v1
	v_lshlrev_b32_e32 v2, 2, v12
	s_waitcnt lgkmcnt(0)
	v_lshl_add_u32 v1, v1, 2, v2
	ds_write_b32 v1, v9
	s_or_b64 exec, exec, s[4:5]
	v_cmp_ne_u32_e32 vcc, -1, v10
	s_and_saveexec_b64 s[4:5], vcc
	s_cbranch_execnz .LBB1_273
.LBB1_280:
	s_or_b64 exec, exec, s[4:5]
	v_cmp_ne_u32_e32 vcc, -1, v13
.Lw1t122:
	s_cbranch_execz .Lw1c122

.Lw1b123:
	s_or_b64 exec, exec, s[4:5]
	v_mov_b32_e32 v1, 0x11ba0
	v_mov_b32_e32 v2, -1
	ds_write_b32 v1, v2
	s_cmp_lt_i32 s3, 1
	s_waitcnt lgkmcnt(0)
	s_barrier
	s_cbranch_scc1 .LBB1_332
	v_lshlrev_b32_e32 v1, 2, v0
	s_lshl_b32 s18, s3, 2
	s_mov_b32 s19, 0x1fffc
	s_mov_b32 s20, 0x10000

.Lw1b124:
	v_mov_b32_e32 v7, 0x11ba0
	v_mov_b32_e32 v2, v0
	v_cmp_gt_i32_e64 s[10:11], s3, v2
	ds_read_b32 v17, v1
	v_mov_b32_e32 v16, v1
	v_add_u32_e32 v2, 1024, v0
	v_cmp_gt_i32_e64 s[12:13], s3, v2
	ds_read_b32 v19, v1 offset:4096

.Lw1b125:
	v_add_u32_e32 v18, 4096, v1
	v_add_u32_e32 v2, 2048, v0
	v_cmp_gt_i32_e64 s[14:15], s3, v2
	ds_read_b32 v21, v1 offset:8192
	v_add_u32_e32 v20, 8192, v1
	v_add_u32_e32 v2, 3072, v0
	v_cmp_gt_i32_e64 s[16:17], s3, v2
	ds_read_b32 v23, v1 offset:12288

.Lw1b126:
	v_add_u32_e32 v22, 12288, v1
	s_waitcnt lgkmcnt(0)
	v_lshrrev_b32_e32 v2, 15, v17
	v_and_b32_e32 v2, s19, v2
	v_lshrrev_b32_e32 v3, 15, v19
	v_and_b32_e32 v3, s19, v3
	v_lshrrev_b32_e32 v4, 15, v21
	v_and_b32_e32 v4, s19, v4
	v_lshrrev_b32_e32 v5, 15, v23
	v_and_b32_e32 v5, s19, v5
	v_cndmask_b32_e64 v2, 0, v2, s[10:11]
	v_add_u32_e32 v2, s20, v2

.Lw1b127:
	v_cndmask_b32_e64 v3, 0, v3, s[12:13]
	v_add_u32_e32 v3, s20, v3
	v_cndmask_b32_e64 v4, 0, v4, s[14:15]
	v_add_u32_e32 v4, s20, v4
	v_cndmask_b32_e64 v5, 0, v5, s[16:17]
	v_add_u32_e32 v5, s20, v5
	ds_read_b32 v24, v2
	ds_read_b32 v28, v2 offset:4096
	ds_read_b32 v25, v3

.Lw1b128:
	ds_read_b32 v29, v3 offset:4096
	ds_read_b32 v26, v4
	ds_read_b32 v30, v4 offset:4096
	ds_read_b32 v27, v5
	ds_read_b32 v31, v5 offset:4096
	s_waitcnt lgkmcnt(0)
	v_cndmask_b32_e64 v2, 0, v24, s[10:11]
	v_lshlrev_b32_e32 v28, 2, v28
	v_mov_b32_e32 v8, v28

.Lw1b129:
	v_mov_b32_e32 v24, 0
	v_cndmask_b32_e64 v3, 0, v25, s[12:13]
	v_lshlrev_b32_e32 v29, 2, v29
	v_mov_b32_e32 v10, v29
	v_mov_b32_e32 v25, 0
	v_cndmask_b32_e64 v4, 0, v26, s[14:15]
	v_lshlrev_b32_e32 v30, 2, v30
	v_mov_b32_e32 v12, v30
	v_mov_b32_e32 v26, 0
	v_cndmask_b32_e64 v5, 0, v27, s[16:17]
	v_lshlrev_b32_e32 v31, 2, v31
	v_mov_b32_e32 v14, v31

.Lw1b130:
	v_mov_b32_e32 v27, 0
	v_max_u32_e32 v6, v2, v3
	v_max3_u32 v6, v6, v4, v5
	s_mov_b32 s21, 0
.Lrs0_loop:
	v_cmp_lt_u32_e32 vcc, s21, v6
	s_cbranch_vccz .Lrs0_done
	v_cmp_gt_u32_e64 s[22:23], s18, v8
	v_cmp_gt_u32_e64 s[24:25], s18, v10
	v_cmp_gt_u32_e64 s[26:27], s18, v12
	v_cmp_gt_u32_e64 s[28:29], s18, v14
.Lw1t131:
	s_cbranch_execz .Lw1c131
.Lw1b131:
	v_cndmask_b32_e64 v2, v7, v8, s[22:23]
	v_cndmask_b32_e64 v3, v7, v10, s[24:25]
	v_cndmask_b32_e64 v4, v7, v12, s[26:27]
	v_cndmask_b32_e64 v5, v7, v14, s[28:29]
	ds_read_b32 v9, v2
	ds_read_b32 v11, v3
	ds_read_b32 v13, v4
	ds_read_b32 v15, v5

.Lw1b132:
	s_waitcnt lgkmcnt(3)
	v_cmp_lt_u64_e64 s[22:23], v[8:9], v[16:17]
	s_waitcnt lgkmcnt(2)
	v_cmp_lt_u64_e64 s[24:25], v[10:11], v[18:19]
	s_waitcnt lgkmcnt(1)
	v_cmp_lt_u64_e64 s[26:27], v[12:13], v[20:21]
	s_waitcnt lgkmcnt(0)
	v_cmp_lt_u64_e64 s[28:29], v[14:15], v[22:23]
	v_addc_co_u32_e64 v24, s[4:5], 0, v24, s[22:23]

.Lw1b133:
	v_addc_co_u32_e64 v25, s[4:5], 0, v25, s[24:25]
	v_addc_co_u32_e64 v26, s[4:5], 0, v26, s[26:27]
	v_addc_co_u32_e64 v27, s[4:5], 0, v27, s[28:29]
	v_add_u32_e32 v8, 4, v8
	v_add_u32_e32 v10, 4, v10
	v_add_u32_e32 v12, 4, v12
	v_add_u32_e32 v14, 4, v14
	s_add_i32 s21, s21, 1
	s_branch .Lrs0_loop
.Lrs0_done:
	v_and_b32_e32 v2, 0x1fffff, v17
	v_lshl_add_u32 v28, v24, 2, v28
.Lw1t134:
	s_cbranch_execz .Lw1c134
.Lw1b134:
	v_and_b32_e32 v3, 0x1fffff, v19
	v_lshl_add_u32 v29, v25, 2, v29
	v_and_b32_e32 v4, 0x1fffff, v21
	v_lshl_add_u32 v30, v26, 2, v30
	v_and_b32_e32 v5, 0x1fffff, v23
	v_lshl_add_u32 v31, v27, 2, v31
	s_mov_b64 exec, s[10:11]
	ds_write_b32 v28, v2 offset:32768

.Lw1b135:
	s_mov_b64 exec, s[12:13]
	ds_write_b32 v29, v3 offset:32768
	s_mov_b64 exec, s[14:15]
	ds_write_b32 v30, v4 offset:32768
	s_mov_b64 exec, s[16:17]
	ds_write_b32 v31, v5 offset:32768
	s_mov_b64 exec, -1
.LBB1_332:
	s_cmpk_lt_i32 s3, 0x1001
	s_cbranch_scc1 .LBB1_382
	v_add_u32_e32 v2, 4096, v0
.Lw1t136:
	s_cbranch_execz .Lw1c136
.Lw1b136:
	v_cmp_gt_i32_e64 s[10:11], s3, v2
	ds_read_b32 v17, v1 offset:16384
	v_add_u32_e32 v16, 16384, v1
	v_add_u32_e32 v2, 5120, v0
	v_cmp_gt_i32_e64 s[12:13], s3, v2
	ds_read_b32 v19, v1 offset:20480
	v_add_u32_e32 v18, 20480, v1
	v_add_u32_e32 v2, 6144, v0

.Lw1b137:
	v_cmp_gt_i32_e64 s[14:15], s3, v2
	ds_read_b32 v21, v1 offset:24576
	v_add_u32_e32 v20, 24576, v1
	v_add_u32_e32 v2, 7168, v0
	v_cmp_gt_i32_e64 s[16:17], s3, v2
	ds_read_b32 v23, v1 offset:28672
	v_add_u32_e32 v22, 28672, v1

.Lw1b138:
	s_waitcnt lgkmcnt(0)
	v_lshrrev_b32_e32 v2, 15, v17
	v_and_b32_e32 v2, s19, v2
	v_lshrrev_b32_e32 v3, 15, v19
	v_and_b32_e32 v3, s19, v3
	v_lshrrev_b32_e32 v4, 15, v21
	v_and_b32_e32 v4, s19, v4
	v_lshrrev_b32_e32 v5, 15, v23
	v_and_b32_e32 v5, s19, v5
	v_cndmask_b32_e64 v2, 0, v2, s[10:11]
	v_add_u32_e32 v2, s20, v2
	v_cndmask_b32_e64 v3, 0, v3, s[12:13]
	v_add_u32_e32 v3, s20, v3

.Lw1b139:
	v_cndmask_b32_e64 v4, 0, v4, s[14:15]
	v_add_u32_e32 v4, s20, v4
	v_cndmask_b32_e64 v5, 0, v5, s[16:17]
	v_add_u32_e32 v5, s20, v5
	ds_read_b32 v24, v2
	ds_read_b32 v28, v2 offset:4096
	ds_read_b32 v25, v3
	ds_read_b32 v29, v3 offset:4096
	ds_read_b32 v26, v4

.Lw1b140:
	ds_read_b32 v30, v4 offset:4096
	ds_read_b32 v27, v5
	ds_read_b32 v31, v5 offset:4096
	s_waitcnt lgkmcnt(0)
	v_cndmask_b32_e64 v2, 0, v24, s[10:11]
	v_lshlrev_b32_e32 v28, 2, v28
	v_mov_b32_e32 v8, v28
	v_mov_b32_e32 v24, 0
	v_cndmask_b32_e64 v3, 0, v25, s[12:13]
.Lw1t141:
	s_cbranch_execz .Lw1c141
.Lw1b141:
	v_lshlrev_b32_e32 v29, 2, v29
	v_mov_b32_e32 v10, v29
	v_mov_b32_e32 v25, 0
	v_cndmask_b32_e64 v4, 0, v26, s[14:15]
	v_lshlrev_b32_e32 v30, 2, v30
	v_mov_b32_e32 v12, v30
	v_mov_b32_e32 v26, 0
	v_cndmask_b32_e64 v5, 0, v27, s[16:17]
	v_lshlrev_b32_e32 v31, 2, v31
	v_mov_b32_e32 v14, v31
	v_mov_b32_e32 v27, 0
	v_max_u32_e32 v6, v2, v3
	v_max3_u32 v6, v6, v4, v5

.Lrs4_done:
	v_and_b32_e32 v2, 0x1fffff, v17
	v_lshl_add_u32 v28, v24, 2, v28
	v_and_b32_e32 v3, 0x1fffff, v19
.Lw1t146:
	s_cbranch_execz .Lw1c146
.Lw1b146:
	v_lshl_add_u32 v29, v25, 2, v29
	v_and_b32_e32 v4, 0x1fffff, v21
	v_lshl_add_u32 v30, v26, 2, v30
	v_and_b32_e32 v5, 0x1fffff, v23
	v_lshl_add_u32 v31, v27, 2, v31
	s_mov_b64 exec, s[10:11]
	ds_write_b32 v28, v2 offset:32768
	s_mov_b64 exec, s[12:13]
	ds_write_b32 v29, v3 offset:32768

.Lw1b147:
	s_mov_b64 exec, s[14:15]
	ds_write_b32 v30, v4 offset:32768
	s_mov_b64 exec, s[16:17]
	ds_write_b32 v31, v5 offset:32768
	s_mov_b64 exec, -1
.LBB1_382:
	s_sub_i32 s4, 0, s34
	s_and_b32 s4, s4, 3
	s_min_i32 s4, s4, s3
	v_cmp_gt_i32_e32 vcc, s4, v0
	s_waitcnt lgkmcnt(0)
	s_barrier
	s_and_saveexec_b64 s[6:7], vcc
.Lw1t148:
	s_cbranch_execz .Lw1c148
.Lw1b148:
	s_cbranch_execz .LBB1_384
	v_lshlrev_b32_e32 v1, 2, v0
	ds_read_b32 v2, v1 offset:32768
	s_waitcnt lgkmcnt(0)
	global_store_dword v1, v2, s[8:9]
.LBB1_384:
	s_or_b64 exec, exec, s[6:7]
	s_sub_i32 s14, s3, s4
	s_ashr_i32 s15, s14, 2
	v_cmp_gt_i32_e32 vcc, s15, v0
	s_and_saveexec_b64 s[6:7], vcc
	s_cbranch_execz .LBB1_387
	s_ashr_i32 s5, s4, 31
	s_lshl_b64 s[10:11], s[4:5], 2
.Lw1t149:
	s_cbranch_execz .Lw1c149
.Lw1b149:
	s_add_u32 s10, s8, s10
	v_lshlrev_b32_e32 v4, 4, v0
	s_addc_u32 s11, s9, s11
	v_mov_b32_e32 v5, 0
	v_lshl_add_u32 v1, s4, 2, v4
	v_lshl_add_u64 v[2:3], s[10:11], 0, v[4:5]
	v_add_u32_e32 v1, 0x8000, v1
	s_mov_b64 s[10:11], 0
	s_mov_b64 s[12:13], 0x4000
	v_mov_b32_e32 v4, v0
.LBB1_386:
	ds_read2_b32 v[6:7], v1 offset1:1
.Lw1t150:
	s_cbranch_execz .Lw1c150
.Lw1b150:
	ds_read2_b32 v[8:9], v1 offset0:2 offset1:3
	v_add_u32_e32 v4, 0x400, v4
	v_cmp_le_i32_e32 vcc, s15, v4
	v_add_u32_e32 v1, 0x4000, v1
	s_or_b64 s[10:11], vcc, s[10:11]
	s_waitcnt lgkmcnt(0)
	global_store_dwordx4 v[2:3], v[6:9], off sc1
	v_lshl_add_u64 v[2:3], v[2:3], 0, s[12:13]
	s_andn2_b64 exec, exec, s[10:11]

.LBB1_387:
	s_or_b64 exec, exec, s[6:7]
	s_and_b32 s6, s14, -4
	s_add_i32 s6, s6, s4
	s_sub_i32 s3, s3, s6
	v_cmp_gt_i32_e32 vcc, s3, v0
	s_and_saveexec_b64 s[4:5], vcc
	s_cbranch_execz .LBB1_389
	v_add_u32_e32 v2, s6, v0
	v_lshlrev_b32_e32 v1, 2, v2
	ds_read_b32 v1, v1 offset:32768
	v_ashrrev_i32_e32 v3, 31, v2
	v_lshl_add_u64 v[2:3], v[2:3], 2, s[8:9]

.Lw1b152:
	s_waitcnt lgkmcnt(0)
	global_store_dword v[2:3], v1, off

.LBB1_390:
.LBB1_394:
	s_endpgm
.Lmy_cvt1:
	s_waitcnt lgkmcnt(0)
	s_load_dwordx4 s[20:23], s[0:1], 0x28
	s_sub_i32 s3, s2, 392
	s_cmp_ge_u32 s3, 291
	s_cbranch_scc1 .Lmy_cvt1_end
	v_and_b32_e32 v1, 0x3c0, v0
.Lw1t153:
	s_cbranch_execz .Lw1c153
.Lw1b153:
	v_and_b32_e32 v2, 63, v0
	v_lshlrev_b32_e32 v3, 5, v1
	v_lshl_or_b32 v3, v2, 4, v3
	v_and_b32_e32 v4, 1, v0
	v_lshrrev_b32_e32 v5, 1, v2
	v_lshl_or_b32 v5, v4, 5, v5
	v_add_u32_e32 v5, v5, v1
	v_lshlrev_b32_e32 v5, 4, v5
	v_cmp_eq_u32_e32 vcc, 0, v4
	s_waitcnt lgkmcnt(0)
	s_add_i32 s8, s3, 400
	s_lshl_b32 s9, s8, 10

.Lw1b154:
	s_sub_i32 s9, 0x1869c0, s9
	v_cmp_ge_i32_e64 s[24:25], s9, v1
	s_add_i32 s8, s3, 691
	s_lshl_b32 s9, s8, 10
	s_sub_i32 s9, 0x1869c0, s9
	v_cmp_ge_i32_e64 s[26:27], s9, v1
	s_add_i32 s8, s3, 982
	s_lshl_b32 s9, s8, 10
	s_sub_i32 s9, 0x1869c0, s9

.Lw1b155:
	v_cmp_ge_i32_e64 s[28:29], s9, v1
	s_add_i32 s8, s3, 1273
	s_lshl_b32 s9, s8, 10
	s_sub_i32 s9, 0x1869c0, s9
	v_cmp_ge_i32_e64 s[30:31], s9, v1
	s_add_i32 s8, s3, 400
	s_lshl_b32 s9, s8, 15
	s_add_u32 s10, s20, s9
	s_addc_u32 s11, s21, 0

.Lw1b156:
	s_mov_b64 exec, s[24:25]
	global_load_dwordx4 v[8:11], v3, s[10:11] nt
	global_load_dwordx4 v[12:15], v3, s[10:11] offset:1024 nt
	s_add_i32 s8, s3, 691
	s_lshl_b32 s9, s8, 15
	s_add_u32 s10, s20, s9
	s_addc_u32 s11, s21, 0
	s_mov_b64 exec, s[26:27]
	global_load_dwordx4 v[16:19], v3, s[10:11] nt
	global_load_dwordx4 v[20:23], v3, s[10:11] offset:1024 nt

.Lw1b157:
	s_add_i32 s8, s3, 982
	s_lshl_b32 s9, s8, 15
	s_add_u32 s10, s20, s9
	s_addc_u32 s11, s21, 0
	s_mov_b64 exec, s[28:29]
	global_load_dwordx4 v[24:27], v3, s[10:11] nt
	global_load_dwordx4 v[28:31], v3, s[10:11] offset:1024 nt
	s_add_i32 s8, s3, 1273
	s_lshl_b32 s9, s8, 15
	s_add_u32 s10, s20, s9
	s_addc_u32 s11, s21, 0

.Lw1b158:
	s_mov_b64 exec, s[30:31]
	global_load_dwordx4 v[32:35], v3, s[10:11] nt
	global_load_dwordx4 v[36:39], v3, s[10:11] offset:1024 nt
	s_waitcnt vmcnt(6)
	s_add_i32 s8, s3, 400
	s_lshl_b32 s9, s8, 14
	s_add_u32 s10, s22, s9
	s_addc_u32 s11, s23, 0
	s_mov_b64 exec, s[24:25]
	v_cvt_pk_f16_f32 v8, v8, v9
	v_cvt_pk_f16_f32 v9, v10, v11

.Lw1b159:
	v_cvt_pk_f16_f32 v10, v12, v13
	v_cvt_pk_f16_f32 v11, v14, v15
	v_cndmask_b32_e32 v12, v8, v10, vcc
	v_cndmask_b32_e32 v13, v9, v11, vcc
	s_nop 1
	v_mov_b32_dpp v12, v12 quad_perm:[1,0,3,2] row_mask:0xf bank_mask:0xf bound_ctrl:1
	v_mov_b32_dpp v13, v13 quad_perm:[1,0,3,2] row_mask:0xf bank_mask:0xf bound_ctrl:1
	v_cndmask_b32_e32 v8, v12, v8, vcc
	v_cndmask_b32_e32 v9, v13, v9, vcc
	v_cndmask_b32_e32 v10, v10, v12, vcc

.Lw1b160:
	v_cndmask_b32_e32 v11, v11, v13, vcc
	global_store_dwordx4 v5, v[8:11], s[10:11] sc1
	s_waitcnt vmcnt(5)
	s_add_i32 s8, s3, 691
	s_lshl_b32 s9, s8, 14
	s_add_u32 s10, s22, s9
	s_addc_u32 s11, s23, 0
	s_mov_b64 exec, s[26:27]
	v_cvt_pk_f16_f32 v16, v16, v17
	v_cvt_pk_f16_f32 v17, v18, v19
	v_cvt_pk_f16_f32 v18, v20, v21

.Lw1b161:
	v_cvt_pk_f16_f32 v19, v22, v23
	v_cndmask_b32_e32 v20, v16, v18, vcc
	v_cndmask_b32_e32 v21, v17, v19, vcc
	s_nop 1
	v_mov_b32_dpp v20, v20 quad_perm:[1,0,3,2] row_mask:0xf bank_mask:0xf bound_ctrl:1
	v_mov_b32_dpp v21, v21 quad_perm:[1,0,3,2] row_mask:0xf bank_mask:0xf bound_ctrl:1
	v_cndmask_b32_e32 v16, v20, v16, vcc
	v_cndmask_b32_e32 v17, v21, v17, vcc
	v_cndmask_b32_e32 v18, v18, v20, vcc
	v_cndmask_b32_e32 v19, v19, v21, vcc
	global_store_dwordx4 v5, v[16:19], s[10:11] sc1

.Lw1b162:
	s_waitcnt vmcnt(4)
	s_add_i32 s8, s3, 982
	s_lshl_b32 s9, s8, 14
	s_add_u32 s10, s22, s9
	s_addc_u32 s11, s23, 0
	s_mov_b64 exec, s[28:29]
	v_cvt_pk_f16_f32 v24, v24, v25
	v_cvt_pk_f16_f32 v25, v26, v27
	v_cvt_pk_f16_f32 v26, v28, v29
	v_cvt_pk_f16_f32 v27, v30, v31

.Lw1b163:
	v_cndmask_b32_e32 v28, v24, v26, vcc
	v_cndmask_b32_e32 v29, v25, v27, vcc
	s_nop 1
	v_mov_b32_dpp v28, v28 quad_perm:[1,0,3,2] row_mask:0xf bank_mask:0xf bound_ctrl:1
	v_mov_b32_dpp v29, v29 quad_perm:[1,0,3,2] row_mask:0xf bank_mask:0xf bound_ctrl:1
	v_cndmask_b32_e32 v24, v28, v24, vcc
	v_cndmask_b32_e32 v25, v29, v25, vcc
	v_cndmask_b32_e32 v26, v26, v28, vcc
	v_cndmask_b32_e32 v27, v27, v29, vcc
	global_store_dwordx4 v5, v[24:27], s[10:11] sc1
	s_waitcnt vmcnt(3)

.Lw1b164:
	s_add_i32 s8, s3, 1273
	s_lshl_b32 s9, s8, 14
	s_add_u32 s10, s22, s9
	s_addc_u32 s11, s23, 0
	s_mov_b64 exec, s[30:31]
	v_cvt_pk_f16_f32 v32, v32, v33
	v_cvt_pk_f16_f32 v33, v34, v35
	v_cvt_pk_f16_f32 v34, v36, v37
	v_cvt_pk_f16_f32 v35, v38, v39
	v_cndmask_b32_e32 v36, v32, v34, vcc

.Lw1b165:
	v_cndmask_b32_e32 v37, v33, v35, vcc
	s_nop 1
	v_mov_b32_dpp v36, v36 quad_perm:[1,0,3,2] row_mask:0xf bank_mask:0xf bound_ctrl:1
	v_mov_b32_dpp v37, v37 quad_perm:[1,0,3,2] row_mask:0xf bank_mask:0xf bound_ctrl:1
	v_cndmask_b32_e32 v32, v36, v32, vcc
	v_cndmask_b32_e32 v33, v37, v33, vcc
	v_cndmask_b32_e32 v34, v34, v36, vcc
	v_cndmask_b32_e32 v35, v35, v37, vcc
	global_store_dwordx4 v5, v[32:35], s[10:11] sc1

	.amdhsa_kernel _Z8k_bucketPKiS0_PKjPiS3_PK15HIP_vector_typeIfLj4EEPS4_IjLj4EE
		.amdhsa_group_segment_fixed_size 72624
		.amdhsa_private_segment_fixed_size 0
		.amdhsa_kernarg_size 56
		.amdhsa_user_sgpr_count 2
		.amdhsa_user_sgpr_dispatch_ptr 0
		.amdhsa_user_sgpr_queue_ptr 0
		.amdhsa_user_sgpr_kernarg_segment_ptr 1
		.amdhsa_user_sgpr_dispatch_id 0
		.amdhsa_user_sgpr_kernarg_preload_length 0
		.amdhsa_user_sgpr_kernarg_preload_offset 0
		.amdhsa_user_sgpr_private_segment_size 0
		.amdhsa_uses_dynamic_stack 0
		.amdhsa_enable_private_segment 0
		.amdhsa_system_sgpr_workgroup_id_x 1
		.amdhsa_system_sgpr_workgroup_id_y 0
		.amdhsa_system_sgpr_workgroup_id_z 0
		.amdhsa_system_sgpr_workgroup_info 0
		.amdhsa_system_vgpr_workitem_id 0
		.amdhsa_next_free_vgpr 48
		.amdhsa_next_free_sgpr 68
		.amdhsa_accum_offset 48
		.amdhsa_reserve_vcc 1
		.amdhsa_float_round_mode_32 0
		.amdhsa_float_round_mode_16_64 0
		.amdhsa_float_denorm_mode_32 3
		.amdhsa_float_denorm_mode_16_64 3
		.amdhsa_dx10_clamp 1
		.amdhsa_ieee_mode 1
		.amdhsa_fp16_overflow 0
		.amdhsa_tg_split 0
		.amdhsa_exception_fp_ieee_invalid_op 0
		.amdhsa_exception_fp_denorm_src 0
		.amdhsa_exception_fp_ieee_div_zero 0
		.amdhsa_exception_fp_ieee_overflow 0
		.amdhsa_exception_fp_ieee_underflow 0
		.amdhsa_exception_fp_ieee_inexact 0
		.amdhsa_exception_int_div_zero 0
	.end_amdhsa_kernel

amdhsa.kernels:
  - .agpr_count:     0
    .args:
      - .actual_access:  read_only
        .address_space:  global
        .offset:         0
        .size:           8
        .value_kind:     global_buffer
      - .actual_access:  read_only
        .address_space:  global
        .offset:         8
        .size:           8
        .value_kind:     global_buffer
      - .actual_access:  write_only
        .address_space:  global
        .offset:         16
        .size:           8
        .value_kind:     global_buffer
      - .actual_access:  write_only
        .address_space:  global
        .offset:         24
        .size:           8
        .value_kind:     global_buffer
      - .actual_access:  write_only
        .address_space:  global
        .offset:         32
        .size:           8
        .value_kind:     global_buffer
      - .actual_access:  read_only
        .address_space:  global
        .offset:         40
        .size:           8
        .value_kind:     global_buffer
      - .actual_access:  read_only
        .address_space:  global
        .offset:         48
        .size:           8
        .value_kind:     global_buffer
      - .actual_access:  read_only
        .address_space:  global
        .offset:         56
        .size:           8
        .value_kind:     global_buffer
      - .actual_access:  write_only
        .address_space:  global
        .offset:         64
        .size:           8
        .value_kind:     global_buffer
      - .actual_access:  write_only
        .address_space:  global
        .offset:         72
        .size:           8
        .value_kind:     global_buffer
      - .actual_access:  read_only
        .address_space:  global
        .offset:         80
        .size:           8
        .value_kind:     global_buffer
      - .address_space:  global
        .offset:         88
        .size:           8
        .value_kind:     global_buffer
      - .actual_access:  write_only
        .address_space:  global
        .offset:         96
        .size:           8
        .value_kind:     global_buffer
    .group_segment_fixed_size: 34400
    .kernarg_segment_align: 8
    .kernarg_segment_size: 104
    .language:       OpenCL C
    .language_version:
      - 2
      - 0
    .max_flat_workgroup_size: 1024
    .name:           _Z7k_frontPKiS0_PiS1_PjPKfS4_S4_P15HIP_vector_typeIjLj4EES7_PKS5_IfLj4EES7_S7_
    .private_segment_fixed_size: 0
    .sgpr_count:     44
    .sgpr_spill_count: 0
    .symbol:         _Z7k_frontPKiS0_PiS1_PjPKfS4_S4_P15HIP_vector_typeIjLj4EES7_PKS5_IfLj4EES7_S7_.kd
    .uniform_work_group_size: 1
    .uses_dynamic_stack: false
    .vgpr_count:     41
    .vgpr_spill_count: 0
    .wavefront_size: 64
  - .agpr_count:     0
    .args:
      - .actual_access:  read_only
        .address_space:  global
        .offset:         0
        .size:           8
        .value_kind:     global_buffer
      - .actual_access:  read_only
        .address_space:  global
        .offset:         8
        .size:           8
        .value_kind:     global_buffer
      - .actual_access:  read_only
        .address_space:  global
        .offset:         16
        .size:           8
        .value_kind:     global_buffer
      - .actual_access:  write_only
        .address_space:  global
        .offset:         24
        .size:           8
        .value_kind:     global_buffer
      - .address_space:  global
        .offset:         32
        .size:           8
        .value_kind:     global_buffer
      - .actual_access:  read_only
        .address_space:  global
        .offset:         40
        .size:           8
        .value_kind:     global_buffer
      - .address_space:  global
        .offset:         48
        .size:           8
        .value_kind:     global_buffer
    .group_segment_fixed_size: 72624
    .kernarg_segment_align: 8
    .kernarg_segment_size: 56
    .language:       OpenCL C
    .language_version:
      - 2
      - 0
    .max_flat_workgroup_size: 1024
    .name:           _Z8k_bucketPKiS0_PKjPiS3_PK15HIP_vector_typeIfLj4EEPS4_IjLj4EE
    .private_segment_fixed_size: 0
    .sgpr_count:     74
    .sgpr_spill_count: 0
    .symbol:         _Z8k_bucketPKiS0_PKjPiS3_PK15HIP_vector_typeIfLj4EEPS4_IjLj4EE.kd
    .uniform_work_group_size: 1
    .uses_dynamic_stack: false
    .vgpr_count:     48
    .vgpr_spill_count: 0
    .wavefront_size: 64
  - .agpr_count:     0
    .args:
      - .actual_access:  read_only
        .address_space:  global
        .offset:         0
        .size:           8
        .value_kind:     global_buffer
      - .actual_access:  read_only
        .address_space:  global
        .offset:         8
        .size:           8
        .value_kind:     global_buffer
      - .actual_access:  read_only
        .address_space:  global
        .offset:         16
        .size:           8
        .value_kind:     global_buffer
      - .actual_access:  read_only
        .address_space:  global
        .offset:         24
        .size:           8
        .value_kind:     global_buffer
      - .actual_access:  read_only
        .address_space:  global
        .offset:         32
        .size:           8
        .value_kind:     global_buffer
      - .actual_access:  read_only
        .address_space:  global
        .offset:         40
        .size:           8
        .value_kind:     global_buffer
      - .actual_access:  read_only
        .address_space:  global
        .offset:         48
        .size:           8
        .value_kind:     global_buffer
      - .actual_access:  read_only
        .address_space:  global
        .offset:         56
        .size:           8
        .value_kind:     global_buffer
      - .actual_access:  read_only
        .address_space:  global
        .offset:         64
        .size:           8
        .value_kind:     global_buffer
      - .actual_access:  read_only
        .address_space:  global
        .offset:         72
        .size:           8
        .value_kind:     global_buffer
      - .actual_access:  read_only
        .address_space:  global
        .offset:         80
        .size:           8
        .value_kind:     global_buffer
      - .actual_access:  write_only
        .address_space:  global
        .offset:         88
        .size:           8
        .value_kind:     global_buffer
      - .actual_access:  read_only
        .address_space:  global
        .offset:         96
        .size:           8
        .value_kind:     global_buffer
      - .offset:         104
        .size:           4
        .value_kind:     hidden_block_count_x
      - .offset:         108
        .size:           4
        .value_kind:     hidden_block_count_y
      - .offset:         112
        .size:           4
        .value_kind:     hidden_block_count_z
      - .offset:         116
        .size:           2
        .value_kind:     hidden_group_size_x
      - .offset:         118
        .size:           2
        .value_kind:     hidden_group_size_y
      - .offset:         120
        .size:           2
        .value_kind:     hidden_group_size_z
      - .offset:         122
        .size:           2
        .value_kind:     hidden_remainder_x
      - .offset:         124
        .size:           2
        .value_kind:     hidden_remainder_y
      - .offset:         126
        .size:           2
        .value_kind:     hidden_remainder_z
      - .offset:         144
        .size:           8
        .value_kind:     hidden_global_offset_x
      - .offset:         152
        .size:           8
        .value_kind:     hidden_global_offset_y
      - .offset:         160
        .size:           8
        .value_kind:     hidden_global_offset_z
      - .offset:         168
        .size:           2
        .value_kind:     hidden_grid_dims
    .group_segment_fixed_size: 125188
    .kernarg_segment_align: 8
    .kernarg_segment_size: 360
    .language:       OpenCL C
    .language_version:
      - 2
      - 0
    .max_flat_workgroup_size: 832
    .name:           _Z10k_layer_a2ILi0ELi13EEvPKDF16_PKiS3_PK15HIP_vector_typeIjLj4EES7_PKfS9_S9_S9_S9_S9_PDF16_Pf
    .private_segment_fixed_size: 0
    .sgpr_count:     58
    .sgpr_spill_count: 0
    .symbol:         _Z10k_layer_a2ILi0ELi13EEvPKDF16_PKiS3_PK15HIP_vector_typeIjLj4EES7_PKfS9_S9_S9_S9_S9_PDF16_Pf.kd
    .uniform_work_group_size: 1
    .uses_dynamic_stack: false
    .vgpr_count:     128
    .vgpr_spill_count: 0
    .wavefront_size: 64
  - .agpr_count:     0
    .args:
      - .actual_access:  read_only
        .address_space:  global
        .offset:         0
        .size:           8
        .value_kind:     global_buffer
      - .actual_access:  read_only
        .address_space:  global
        .offset:         8
        .size:           8
        .value_kind:     global_buffer
      - .actual_access:  read_only
        .address_space:  global
        .offset:         16
        .size:           8
        .value_kind:     global_buffer
      - .actual_access:  read_only
        .address_space:  global
        .offset:         24
        .size:           8
        .value_kind:     global_buffer
      - .actual_access:  read_only
        .address_space:  global
        .offset:         32
        .size:           8
        .value_kind:     global_buffer
      - .actual_access:  read_only
        .address_space:  global
        .offset:         40
        .size:           8
        .value_kind:     global_buffer
      - .actual_access:  read_only
        .address_space:  global
        .offset:         48
        .size:           8
        .value_kind:     global_buffer
      - .actual_access:  read_only
        .address_space:  global
        .offset:         56
        .size:           8
        .value_kind:     global_buffer
      - .actual_access:  read_only
        .address_space:  global
        .offset:         64
        .size:           8
        .value_kind:     global_buffer
      - .actual_access:  read_only
        .address_space:  global
        .offset:         72
        .size:           8
        .value_kind:     global_buffer
      - .actual_access:  read_only
        .address_space:  global
        .offset:         80
        .size:           8
        .value_kind:     global_buffer
      - .actual_access:  read_only
        .address_space:  global
        .offset:         88
        .size:           8
        .value_kind:     global_buffer
      - .actual_access:  write_only
        .address_space:  global
        .offset:         96
        .size:           8
        .value_kind:     global_buffer
      - .offset:         104
        .size:           4
        .value_kind:     hidden_block_count_x
      - .offset:         108
        .size:           4
        .value_kind:     hidden_block_count_y
      - .offset:         112
        .size:           4
        .value_kind:     hidden_block_count_z
      - .offset:         116
        .size:           2
        .value_kind:     hidden_group_size_x
      - .offset:         118
        .size:           2
        .value_kind:     hidden_group_size_y
      - .offset:         120
        .size:           2
        .value_kind:     hidden_group_size_z
      - .offset:         122
        .size:           2
        .value_kind:     hidden_remainder_x
      - .offset:         124
        .size:           2
        .value_kind:     hidden_remainder_y
      - .offset:         126
        .size:           2
        .value_kind:     hidden_remainder_z
      - .offset:         144
        .size:           8
        .value_kind:     hidden_global_offset_x
      - .offset:         152
        .size:           8
        .value_kind:     hidden_global_offset_y
      - .offset:         160
        .size:           8
        .value_kind:     hidden_global_offset_z
      - .offset:         168
        .size:           2
        .value_kind:     hidden_grid_dims
    .group_segment_fixed_size: 162052
    .kernarg_segment_align: 8
    .kernarg_segment_size: 360
    .language:       OpenCL C
    .language_version:
      - 2
      - 0
    .max_flat_workgroup_size: 832
    .name:           _Z10k_layer_a2ILi1ELi13EEvPKDF16_PKiS3_PK15HIP_vector_typeIjLj4EES7_PKfS9_S9_S9_S9_S9_PDF16_Pf
    .private_segment_fixed_size: 0
    .sgpr_count:     58
    .sgpr_spill_count: 0
    .symbol:         _Z10k_layer_a2ILi1ELi13EEvPKDF16_PKiS3_PK15HIP_vector_typeIjLj4EES7_PKfS9_S9_S9_S9_S9_PDF16_Pf.kd
    .uniform_work_group_size: 1
    .uses_dynamic_stack: false
    .vgpr_count:     125
    .vgpr_spill_count: 0
    .wavefront_size: 64
